# v59 + MLA/NA QK^T: one counted LDS wait per MFMA pair (23 waits fewer between back-to-back MFMAs); GQA loop head kept 8-byte aligned
# speedup vs baseline: 1.0079x; 1.0035x over previous
.LBB0_814:
	s_add_i32 s24, s23, -3
	ds_read_b128 v[64:67], v198 offset:49152
	ds_read_b128 v[68:71], v198 offset:57344
	ds_read_b128 v[212:215], v200 offset:49152
	ds_read_b128 v[216:219], v200 offset:57344
	v_exp_f32_e32 v160, v160
	v_exp_f32_e32 v161, v161
	s_waitcnt lgkmcnt(3)
	v_mfma_f32_32x32x16_bf16 v[80:95], v[64:67], v[120:123], 0
	v_exp_f32_e32 v152, v152
	v_exp_f32_e32 v153, v153
	v_exp_f32_e32 v158, v158
	v_exp_f32_e32 v150, v150
	v_exp_f32_e32 v159, v159
	v_exp_f32_e32 v151, v151
	v_exp_f32_e32 v156, v156
	s_waitcnt lgkmcnt(2)
	v_mfma_f32_32x32x16_bf16 v[64:79], v[68:71], v[120:123], 0
	v_exp_f32_e32 v148, v148
	v_exp_f32_e32 v157, v157
	v_exp_f32_e32 v149, v149
	v_add_f32_e32 v162, v176, v211
	v_add_f32_e32 v180, v166, v173
	v_add_f32_e32 v194, v160, v161
	v_add_f32_e32 v195, v152, v153
	s_waitcnt lgkmcnt(1)
	v_mfma_f32_32x32x16_bf16 v[80:95], v[212:215], v[124:127], v[80:95]
	v_exp_f32_e32 v154, v154
	v_exp_f32_e32 v146, v146
	v_add_f32_e32 v162, v163, v162
	v_add_f32_e32 v180, v167, v180
	v_add_f32_e32 v194, v158, v194
	v_add_f32_e32 v195, v150, v195
	v_exp_f32_e32 v155, v155
	s_waitcnt lgkmcnt(0)
	v_mfma_f32_32x32x16_bf16 v[64:79], v[216:219], v[124:127], v[64:79]
	ds_read_b128 v[212:215], v199 offset:49152
	ds_read_b128 v[216:219], v199 offset:57344
	v_exp_f32_e32 v147, v147
	v_add_f32_e32 v162, v177, v162
	v_add_f32_e32 v180, v172, v180
	v_add_f32_e32 v194, v159, v194
	v_add_f32_e32 v195, v151, v195
	v_add_f32_e32 v162, v164, v162
	s_waitcnt lgkmcnt(1)
	v_mfma_f32_32x32x16_bf16 v[80:95], v[212:215], v[116:119], v[80:95]
	v_add_f32_e32 v180, v168, v180
	v_add_f32_e32 v194, v156, v194
	v_add_f32_e32 v195, v148, v195
	v_add_f32_e32 v162, v175, v162
	v_add_f32_e32 v180, v171, v180
	v_add_f32_e32 v194, v157, v194
	v_add_f32_e32 v195, v149, v195
	s_waitcnt lgkmcnt(0)
	v_mfma_f32_32x32x16_bf16 v[64:79], v[216:219], v[116:119], v[64:79]
	ds_read_b128 v[212:215], v193 offset:49152
	ds_read_b128 v[216:219], v193 offset:57344
	v_add_f32_e32 v162, v165, v162
	v_add_f32_e32 v180, v169, v180
	v_add_f32_e32 v194, v154, v194
	v_add_f32_e32 v195, v146, v195
	v_add_f32_e32 v162, v174, v162
	s_waitcnt lgkmcnt(1)
	v_mfma_f32_32x32x16_bf16 v[80:95], v[212:215], v[112:115], v[80:95]
	v_add_f32_e32 v180, v170, v180
	v_add_f32_e32 v194, v155, v194
	v_add_f32_e32 v195, v147, v195
	v_add_f32_e32 v162, v180, v162
	v_add_f32_e32 v180, v195, v194
	v_add_f32_e32 v209, v162, v180
	v_mov_b32_e32 v210, v209
	s_waitcnt lgkmcnt(0)
	v_mfma_f32_32x32x16_bf16 v[64:79], v[216:219], v[112:115], v[64:79]
	ds_read_b128 v[212:215], v192 offset:49152
	ds_read_b128 v[216:219], v192 offset:57344
	v_permlane32_swap_b32_e32 v209, v210
	s_waitcnt lgkmcnt(0)
	v_mfma_f32_32x32x16_bf16 v[80:95], v[212:215], v[108:111], v[80:95]
	v_mfma_f32_32x32x16_bf16 v[64:79], v[216:219], v[108:111], v[64:79]
	ds_read_b128 v[212:215], v191 offset:49152
	ds_read_b128 v[216:219], v191 offset:57344
	s_waitcnt lgkmcnt(0)
	v_mfma_f32_32x32x16_bf16 v[80:95], v[212:215], v[104:107], v[80:95]
	v_mfma_f32_32x32x16_bf16 v[64:79], v[216:219], v[104:107], v[64:79]
	ds_read_b128 v[212:215], v190 offset:49152
	ds_read_b128 v[216:219], v190 offset:57344
	s_waitcnt lgkmcnt(0)
	v_mfma_f32_32x32x16_bf16 v[80:95], v[212:215], v[100:103], v[80:95]
	v_mfma_f32_32x32x16_bf16 v[64:79], v[216:219], v[100:103], v[64:79]
	ds_read_b128 v[212:215], v189 offset:49152
	ds_read_b128 v[216:219], v189 offset:57344
	v_cvt_pk_bf16_f32 v162, v176, v211
	v_cvt_pk_bf16_f32 v163, v163, v177
	v_cvt_pk_bf16_f32 v164, v164, v175
	v_cvt_pk_bf16_f32 v165, v165, v174
	v_cvt_pk_bf16_f32 v166, v166, v173
	v_cvt_pk_bf16_f32 v167, v167, v172
	s_waitcnt lgkmcnt(1)
	v_mfma_f32_32x32x16_bf16 v[80:95], v[212:215], v[96:99], v[80:95]
	v_cvt_pk_bf16_f32 v168, v168, v171
	v_cvt_pk_bf16_f32 v169, v169, v170
	v_cvt_pk_bf16_f32 v170, v160, v161
	v_cvt_pk_bf16_f32 v171, v158, v159
	v_cvt_pk_bf16_f32 v172, v156, v157
	v_cvt_pk_bf16_f32 v173, v154, v155
	v_cvt_pk_bf16_f32 v174, v152, v153
	s_waitcnt lgkmcnt(0)
	v_mfma_f32_32x32x16_bf16 v[64:79], v[216:219], v[96:99], v[64:79]
	v_cvt_pk_bf16_f32 v175, v150, v151
	v_cvt_pk_bf16_f32 v176, v148, v149
	v_cvt_pk_bf16_f32 v177, v146, v147
	s_cmp_gt_u32 s24, 1
	s_mov_b64 s[10:11], -1
	s_cbranch_scc0 .LBB0_816
	s_add_i32 s25, s17, s23
	s_add_i32 s2, s25, -5
	s_min_i32 s2, s2, s18
	s_lshl_b32 s2, s2, 6
	s_addk_i32 s2, 0x100
	s_mov_b64 s[10:11], 0

.LBB0_825:
	v_cndmask_b32_e64 v206, v65, v206, s[58:59]
	v_mul_f32_e32 v138, 0xbe0293ee, v206
	v_fmamk_f32 v65, v162, 0x3e0293ee, v138
	v_fmamk_f32 v66, v163, 0x3e0293ee, v138
	v_fmamk_f32 v67, v164, 0x3e0293ee, v138
	v_fmamk_f32 v68, v165, 0x3e0293ee, v138
	v_fmamk_f32 v69, v166, 0x3e0293ee, v138
	v_fmamk_f32 v70, v167, 0x3e0293ee, v138
	v_fmamk_f32 v73, v168, 0x3e0293ee, v138
	v_fmamk_f32 v74, v169, 0x3e0293ee, v138
	v_fmamk_f32 v75, v170, 0x3e0293ee, v138
	v_fmamk_f32 v76, v171, 0x3e0293ee, v138
	v_fmamk_f32 v77, v172, 0x3e0293ee, v138
	v_fmamk_f32 v78, v173, 0x3e0293ee, v138
	v_fmamk_f32 v80, v174, 0x3e0293ee, v138
	v_fmamk_f32 v81, v175, 0x3e0293ee, v138
	v_fmamk_f32 v82, v176, 0x3e0293ee, v138
	v_fmamk_f32 v83, v177, 0x3e0293ee, v138
	v_exp_f32_e32 v170, v65
	v_exp_f32_e32 v171, v66
	v_exp_f32_e32 v172, v67
	v_exp_f32_e32 v173, v68
	v_exp_f32_e32 v174, v69
	v_exp_f32_e32 v175, v70
	v_exp_f32_e32 v176, v73
	v_exp_f32_e32 v177, v74
	v_fmamk_f32 v162, v71, 0x3e0293ee, v138
	v_fmamk_f32 v163, v72, 0x3e0293ee, v138
	v_fmamk_f32 v164, v217, 0x3e0293ee, v138
	v_fmamk_f32 v165, v218, 0x3e0293ee, v138
	v_fmamk_f32 v166, v219, 0x3e0293ee, v138
	v_fmamk_f32 v167, v220, 0x3e0293ee, v138
	v_fmamk_f32 v168, v221, 0x3e0293ee, v138
	v_fmamk_f32 v169, v222, 0x3e0293ee, v138
	v_fmamk_f32 v139, v64, 0x3e0293ee, v138
	v_fmamk_f32 v140, v211, 0x3e0293ee, v138
	v_fmamk_f32 v141, v212, 0x3e0293ee, v138
	v_fmamk_f32 v142, v213, 0x3e0293ee, v138
	v_fmamk_f32 v143, v214, 0x3e0293ee, v138
	v_fmamk_f32 v144, v215, 0x3e0293ee, v138
	v_fmamk_f32 v145, v216, 0x3e0293ee, v138
	v_fmac_f32_e32 v138, 0x3e0293ee, v79
	v_exp_f32_e32 v194, v75
	v_exp_f32_e32 v195, v76
	v_exp_f32_e32 v196, v77
	v_exp_f32_e32 v197, v78
	v_exp_f32_e32 v211, v80
	v_exp_f32_e32 v214, v81
	v_exp_f32_e32 v215, v82
	v_exp_f32_e32 v216, v83
	s_waitcnt lgkmcnt(0)
	s_barrier
	ds_read_b128 v[64:67], v198 offset:32768
	ds_read_b128 v[68:71], v198 offset:40960
	ds_read_b128 v[130:133], v200 offset:32768
	ds_read_b128 v[134:137], v200 offset:40960
	v_exp_f32_e32 v138, v138
	s_waitcnt lgkmcnt(2)
	v_mfma_f32_32x32x16_bf16 v[80:95], v[64:67], v[120:123], 0
	v_mfma_f32_32x32x16_bf16 v[64:79], v[68:71], v[120:123], 0
	s_waitcnt lgkmcnt(0)
	v_mfma_f32_32x32x16_bf16 v[80:95], v[130:133], v[124:127], v[80:95]
	v_mfma_f32_32x32x16_bf16 v[64:79], v[134:137], v[124:127], v[64:79]
	ds_read_b128 v[130:133], v199 offset:32768
	ds_read_b128 v[134:137], v199 offset:40960
	s_waitcnt lgkmcnt(0)
	v_mfma_f32_32x32x16_bf16 v[80:95], v[130:133], v[116:119], v[80:95]
	v_mfma_f32_32x32x16_bf16 v[64:79], v[134:137], v[116:119], v[64:79]
	ds_read_b128 v[130:133], v193 offset:32768
	ds_read_b128 v[134:137], v193 offset:40960
	s_waitcnt lgkmcnt(0)
	v_mfma_f32_32x32x16_bf16 v[80:95], v[130:133], v[112:115], v[80:95]
	v_mfma_f32_32x32x16_bf16 v[64:79], v[134:137], v[112:115], v[64:79]
	ds_read_b128 v[130:133], v192 offset:32768
	ds_read_b128 v[134:137], v192 offset:40960
	s_waitcnt lgkmcnt(0)
	v_mfma_f32_32x32x16_bf16 v[80:95], v[130:133], v[108:111], v[80:95]
	v_mfma_f32_32x32x16_bf16 v[64:79], v[134:137], v[108:111], v[64:79]
	ds_read_b128 v[130:133], v191 offset:32768
	ds_read_b128 v[134:137], v191 offset:40960
	s_waitcnt lgkmcnt(0)
	v_mfma_f32_32x32x16_bf16 v[80:95], v[130:133], v[104:107], v[80:95]
	v_mfma_f32_32x32x16_bf16 v[64:79], v[134:137], v[104:107], v[64:79]
	ds_read_b128 v[130:133], v190 offset:32768
	ds_read_b128 v[134:137], v190 offset:40960
	s_waitcnt lgkmcnt(0)
	v_mfma_f32_32x32x16_bf16 v[80:95], v[130:133], v[100:103], v[80:95]
	v_mfma_f32_32x32x16_bf16 v[64:79], v[134:137], v[100:103], v[64:79]
	ds_read_b128 v[130:133], v189 offset:32768
	ds_read_b128 v[134:137], v189 offset:40960
	s_waitcnt lgkmcnt(1)
	v_mfma_f32_32x32x16_bf16 v[80:95], v[130:133], v[96:99], v[80:95]
	v_exp_f32_e32 v130, v139
	v_exp_f32_e32 v131, v140
	v_exp_f32_e32 v139, v163
	v_exp_f32_e32 v140, v164
	v_exp_f32_e32 v132, v141
	v_exp_f32_e32 v141, v165
	v_exp_f32_e32 v133, v142
	v_exp_f32_e32 v142, v166
	s_waitcnt lgkmcnt(0)
	v_mfma_f32_32x32x16_bf16 v[64:79], v[134:137], v[96:99], v[64:79]
	v_exp_f32_e32 v134, v143
	v_exp_f32_e32 v143, v167
	v_exp_f32_e32 v135, v144
	v_exp_f32_e32 v137, v162
	v_exp_f32_e32 v144, v168
	v_add_f32_e32 v162, v170, v171
	v_add_f32_e32 v163, v194, v195
	v_add_f32_e32 v164, v130, v131
	v_add_f32_e32 v165, v139, v140
	v_exp_f32_e32 v136, v145
	v_exp_f32_e32 v145, v169
	v_add_f32_e32 v162, v172, v162
	v_add_f32_e32 v163, v196, v163
	v_add_f32_e32 v164, v132, v164
	v_add_f32_e32 v165, v141, v165
	v_add_f32_e32 v162, v173, v162
	v_add_f32_e32 v163, v197, v163
	v_add_f32_e32 v164, v133, v164
	v_add_f32_e32 v165, v142, v165
	v_add_f32_e32 v162, v174, v162
	v_add_f32_e32 v163, v211, v163
	v_add_f32_e32 v164, v134, v164
	v_add_f32_e32 v165, v143, v165
	v_add_f32_e32 v162, v175, v162
	v_add_f32_e32 v163, v214, v163
	v_add_f32_e32 v164, v135, v164
	v_add_f32_e32 v165, v144, v165
	v_add_f32_e32 v162, v176, v162
	v_add_f32_e32 v163, v215, v163
	v_add_f32_e32 v164, v136, v164
	v_add_f32_e32 v165, v145, v165
	v_add_f32_e32 v162, v177, v162
	v_add_f32_e32 v163, v216, v163
	v_add_f32_e32 v164, v137, v164
	v_add_f32_e32 v165, v138, v165
	v_add_f32_e32 v162, v163, v162
	v_add_f32_e32 v163, v165, v164
	v_add_f32_e32 v212, v163, v162
	v_mov_b32_e32 v213, v212
	v_cvt_pk_bf16_f32 v162, v170, v171
	v_cvt_pk_bf16_f32 v163, v172, v173
	v_cvt_pk_bf16_f32 v164, v174, v175
	v_cvt_pk_bf16_f32 v165, v176, v177
	v_cvt_pk_bf16_f32 v166, v194, v195
	v_cvt_pk_bf16_f32 v167, v196, v197
	v_cvt_pk_bf16_f32 v168, v211, v214
	v_cvt_pk_bf16_f32 v169, v215, v216
	v_cvt_pk_bf16_f32 v170, v130, v131
	v_cvt_pk_bf16_f32 v171, v132, v133
	v_cvt_pk_bf16_f32 v172, v134, v135
	v_cvt_pk_bf16_f32 v173, v136, v137
	v_cvt_pk_bf16_f32 v174, v139, v140
	v_cvt_pk_bf16_f32 v175, v141, v142
	v_cvt_pk_bf16_f32 v176, v143, v144
	v_cvt_pk_bf16_f32 v177, v145, v138
	s_nop 1
	v_permlane32_swap_b32_e32 v212, v213
	s_min_i32 s3, s23, s21
	s_cmp_gt_i32 s3, 3
	s_mov_b64 s[10:11], -1
	s_cbranch_scc0 .LBB0_827
	s_add_i32 s2, s3, s20
	s_min_i32 s2, s2, s18
	s_lshl_b32 s2, s2, 6
	s_addk_i32 s2, 0x100
	s_mov_b64 s[10:11], 0

.LBB0_861:
	ds_read_b128 v[96:99], v209 offset:49152
	ds_read_b128 v[100:103], v209 offset:57344
	ds_read_b128 v[162:165], v211 offset:49152
	ds_read_b128 v[166:169], v211 offset:57344
	s_add_i32 s2, 0, 0x12000
	v_add_u32_e32 v233, s2, v218
	s_waitcnt lgkmcnt(3)
	v_mfma_f32_32x32x16_bf16 v[112:127], v[96:99], v[158:161], 0
	v_add_u32_e32 v234, s2, v220
	v_add_u32_e32 v236, s2, v222
	v_add_u32_e32 v235, s2, v224
	v_exp_f32_e32 v80, v80
	v_exp_f32_e32 v81, v81
	v_exp_f32_e32 v82, v82
	v_exp_f32_e32 v83, v83
	s_waitcnt lgkmcnt(2)
	v_mfma_f32_32x32x16_bf16 v[96:111], v[100:103], v[158:161], 0
	v_exp_f32_e32 v84, v84
	v_exp_f32_e32 v92, v92
	v_exp_f32_e32 v85, v85
	v_exp_f32_e32 v93, v93
	v_exp_f32_e32 v86, v86
	v_exp_f32_e32 v94, v94
	v_exp_f32_e32 v87, v87
	s_waitcnt lgkmcnt(1)
	v_mfma_f32_32x32x16_bf16 v[112:127], v[162:165], v[154:157], v[112:127]
	v_exp_f32_e32 v95, v95
	s_waitcnt lgkmcnt(0)
	v_mfma_f32_32x32x16_bf16 v[96:111], v[166:169], v[154:157], v[96:111]
	ds_read_b128 v[162:165], v212 offset:49152
	ds_read_b128 v[166:169], v212 offset:57344
	s_waitcnt lgkmcnt(0)
	v_mfma_f32_32x32x16_bf16 v[112:127], v[162:165], v[150:153], v[112:127]
	v_mfma_f32_32x32x16_bf16 v[96:111], v[166:169], v[150:153], v[96:111]
	ds_read_b128 v[162:165], v213 offset:49152
	ds_read_b128 v[166:169], v213 offset:57344
	s_waitcnt lgkmcnt(0)
	v_mfma_f32_32x32x16_bf16 v[112:127], v[162:165], v[146:149], v[112:127]
	v_mfma_f32_32x32x16_bf16 v[96:111], v[166:169], v[146:149], v[96:111]
	ds_read_b128 v[162:165], v215 offset:49152
	ds_read_b128 v[166:169], v215 offset:57344
	s_waitcnt lgkmcnt(0)
	v_mfma_f32_32x32x16_bf16 v[112:127], v[162:165], v[142:145], v[112:127]
	v_mfma_f32_32x32x16_bf16 v[96:111], v[166:169], v[142:145], v[96:111]
	ds_read_b128 v[162:165], v217 offset:49152
	ds_read_b128 v[166:169], v217 offset:57344
	s_waitcnt lgkmcnt(0)
	v_mfma_f32_32x32x16_bf16 v[112:127], v[162:165], v[138:141], v[112:127]
	v_mfma_f32_32x32x16_bf16 v[96:111], v[166:169], v[138:141], v[96:111]
	ds_read_b128 v[162:165], v214 offset:49152
	ds_read_b128 v[166:169], v214 offset:57344
	s_waitcnt lgkmcnt(0)
	v_mfma_f32_32x32x16_bf16 v[112:127], v[162:165], v[134:137], v[112:127]
	v_mfma_f32_32x32x16_bf16 v[96:111], v[166:169], v[134:137], v[96:111]
	ds_read_b128 v[162:165], v216 offset:49152
	ds_read_b128 v[166:169], v216 offset:57344
	s_waitcnt lgkmcnt(0)
	v_mfma_f32_32x32x16_bf16 v[112:127], v[162:165], v[130:133], v[112:127]
	v_mfma_f32_32x32x16_bf16 v[96:111], v[166:169], v[130:133], v[96:111]
	ds_read_b128 v[162:165], v233
	ds_read_b128 v[166:169], v233 offset:4096
	ds_read_b128 v[170:173], v204
	s_waitcnt lgkmcnt(0)
	v_mfma_f32_32x32x16_bf16 v[112:127], v[162:165], v[170:173], v[112:127]
	v_mfma_f32_32x32x16_bf16 v[96:111], v[166:169], v[170:173], v[96:111]
	ds_read_b128 v[162:165], v234
	ds_read_b128 v[166:169], v234 offset:4096
	ds_read_b128 v[170:173], v204 offset:1024
	s_waitcnt lgkmcnt(0)
	v_mfma_f32_32x32x16_bf16 v[112:127], v[162:165], v[170:173], v[112:127]
	v_mfma_f32_32x32x16_bf16 v[96:111], v[166:169], v[170:173], v[96:111]
	ds_read_b128 v[162:165], v236
	ds_read_b128 v[166:169], v236 offset:4096
	ds_read_b128 v[170:173], v204 offset:2048
	s_waitcnt lgkmcnt(0)
	v_mfma_f32_32x32x16_bf16 v[112:127], v[162:165], v[170:173], v[112:127]
	v_mfma_f32_32x32x16_bf16 v[96:111], v[166:169], v[170:173], v[96:111]
	ds_read_b128 v[162:165], v235
	ds_read_b128 v[166:169], v235 offset:4096
	ds_read_b128 v[170:173], v204 offset:3072
	s_waitcnt lgkmcnt(0)
	v_mfma_f32_32x32x16_bf16 v[112:127], v[162:165], v[170:173], v[112:127]
	v_exp_f32_e32 v162, v88
	v_exp_f32_e32 v163, v89
	v_exp_f32_e32 v164, v90
	v_exp_f32_e32 v165, v91
	v_add_f32_e32 v88, v64, v65
	v_add_f32_e32 v89, v72, v73
	v_add_f32_e32 v90, v80, v81
	v_add_f32_e32 v91, v162, v163
	v_add_f32_e32 v88, v66, v88
	v_add_f32_e32 v89, v74, v89
	v_add_f32_e32 v90, v82, v90
	v_add_f32_e32 v91, v164, v91
	v_add_f32_e32 v88, v67, v88
	v_add_f32_e32 v89, v75, v89
	v_add_f32_e32 v90, v83, v90
	v_add_f32_e32 v91, v165, v91
	v_add_f32_e32 v88, v68, v88
	v_add_f32_e32 v89, v76, v89
	v_add_f32_e32 v90, v84, v90
	v_add_f32_e32 v91, v92, v91
	v_add_f32_e32 v88, v69, v88
	v_add_f32_e32 v89, v77, v89
	v_add_f32_e32 v90, v85, v90
	v_add_f32_e32 v91, v93, v91
	v_add_f32_e32 v88, v70, v88
	v_add_f32_e32 v89, v78, v89
	v_add_f32_e32 v90, v86, v90
	v_add_f32_e32 v91, v94, v91
	v_add_f32_e32 v88, v71, v88
	v_add_f32_e32 v89, v79, v89
	v_add_f32_e32 v90, v87, v90
	v_add_f32_e32 v91, v95, v91
	v_add_f32_e32 v88, v89, v88
	v_add_f32_e32 v89, v91, v90
	v_add_f32_e32 v237, v88, v89
	v_cvt_pk_bf16_f32 v88, v64, v65
	v_cvt_pk_bf16_f32 v89, v66, v67
	v_cvt_pk_bf16_f32 v90, v68, v69
	v_cvt_pk_bf16_f32 v91, v70, v71
	v_cvt_pk_bf16_f32 v72, v72, v73
	v_cvt_pk_bf16_f32 v73, v74, v75
	v_cvt_pk_bf16_f32 v74, v76, v77
	v_cvt_pk_bf16_f32 v75, v78, v79
	v_cvt_pk_bf16_f32 v64, v80, v81
	v_cvt_pk_bf16_f32 v65, v82, v83
	v_cvt_pk_bf16_f32 v66, v84, v85
	v_cvt_pk_bf16_f32 v67, v86, v87
	v_cvt_pk_bf16_f32 v68, v162, v163
	v_cvt_pk_bf16_f32 v69, v164, v165
	v_cvt_pk_bf16_f32 v70, v92, v93
	v_cvt_pk_bf16_f32 v71, v94, v95
	v_mfma_f32_32x32x16_bf16 v[96:111], v[166:169], v[170:173], v[96:111]
	v_lshl_add_u64 v[80:81], v[190:191], 0, s[6:7]
	global_load_dwordx4 v[162:165], v[80:81], off
	v_lshl_add_u64 v[80:81], v[192:193], 0, s[6:7]
	v_lshl_add_u64 v[76:77], v[188:189], 0, s[6:7]
	global_load_dwordx4 v[166:169], v[80:81], off
	v_lshl_add_u64 v[80:81], v[198:199], 0, s[6:7]
	global_load_dwordx4 v[76:79], v[76:77], off
	s_nop 0
	global_load_dwordx4 v[174:177], v[80:81], off
	global_load_dwordx4 v[170:173], v[186:187], off
	ds_read_b64_tr_b16 v[80:81], v201 offset:0
	ds_read_b64_tr_b16 v[82:83], v201 offset:0x800
	ds_read_b64_tr_b16 v[84:85], v201 offset:0x1000
	ds_read_b64_tr_b16 v[86:87], v201 offset:0x1800
	ds_read_b64_tr_b16 v[92:93], v201 offset:0x2000
	ds_read_b64_tr_b16 v[94:95], v201 offset:0x2800
	ds_read_b64_tr_b16 v[178:179], v201 offset:0x3000
	ds_read_b64_tr_b16 v[180:181], v201 offset:0x3800
	s_waitcnt lgkmcnt(0)
	s_nop 0
	v_mfma_f32_32x32x16_bf16 v[0:15], v[80:83], v[88:91], v[0:15]
	v_max_f32_e32 v80, v96, v97
	v_max3_f32 v81, v112, v113, v114
	v_max3_f32 v80, v80, v98, v99
	v_max3_f32 v81, v81, v115, v116
	v_max3_f32 v80, v80, v100, v101
	v_mfma_f32_32x32x16_bf16 v[0:15], v[84:87], v[72:75], v[0:15]
	v_max3_f32 v81, v81, v117, v118
	v_max3_f32 v80, v80, v102, v103
	v_max3_f32 v81, v81, v119, v120
	v_max3_f32 v80, v80, v104, v105
	v_max3_f32 v81, v81, v121, v122
	v_max3_f32 v80, v80, v106, v107
	v_max3_f32 v81, v81, v123, v124
	v_mfma_f32_32x32x16_bf16 v[0:15], v[92:95], v[64:67], v[0:15]
	v_max3_f32 v80, v80, v108, v109
	v_max3_f32 v81, v81, v125, v126
	v_max3_f32 v80, v80, v110, v111
	v_max3_f32 v194, v81, v127, v80
	ds_read_b64_tr_b16 v[80:81], v201 offset:0x200
	ds_read_b64_tr_b16 v[82:83], v201 offset:0xa00
	ds_read_b64_tr_b16 v[84:85], v201 offset:0x1200
	v_mfma_f32_32x32x16_bf16 v[0:15], v[178:181], v[68:71], v[0:15]
	ds_read_b64_tr_b16 v[86:87], v201 offset:0x1a00
	ds_read_b64_tr_b16 v[92:93], v201 offset:0x2200
	ds_read_b64_tr_b16 v[94:95], v201 offset:0x2a00
	ds_read_b64_tr_b16 v[178:179], v201 offset:0x3200
	ds_read_b64_tr_b16 v[180:181], v201 offset:0x3a00
	s_waitcnt lgkmcnt(0)
	v_mfma_f32_32x32x16_bf16 v[48:63], v[80:83], v[88:91], v[48:63]
	v_mov_b32_e32 v80, v194
	s_nop 1
	v_permlane32_swap_b32_e32 v194, v80
	v_max_f32_e32 v80, v194, v80
	v_sub_f32_e32 v81, v80, v227
	v_mfma_f32_32x32x16_bf16 v[48:63], v[84:87], v[72:75], v[48:63]
	v_cmp_ge_f32_e32 vcc, s34, v81
	v_mov_b32_e32 v202, 1.0
	s_cmp_eq_u64 vcc, exec
	s_cbranch_scc0 .Lmla_resc_0

.LBB0_863:
	s_waitcnt lgkmcnt(0)
	s_barrier
	ds_read_b128 v[64:67], v209 offset:32768
	ds_read_b128 v[68:71], v209 offset:40960
	ds_read_b128 v[162:165], v211 offset:32768
	ds_read_b128 v[166:169], v211 offset:40960
	v_exp_f32_e32 v112, v112
	v_exp_f32_e32 v113, v113
	s_waitcnt lgkmcnt(3)
	v_mfma_f32_32x32x16_bf16 v[96:111], v[64:67], v[158:161], 0
	v_exp_f32_e32 v114, v114
	v_exp_f32_e32 v115, v115
	v_exp_f32_e32 v116, v116
	v_exp_f32_e32 v117, v117
	v_exp_f32_e32 v118, v118
	v_exp_f32_e32 v119, v119
	s_waitcnt lgkmcnt(1)
	v_mfma_f32_32x32x16_bf16 v[64:79], v[68:71], v[158:161], 0
	v_mfma_f32_32x32x16_bf16 v[96:111], v[162:165], v[154:157], v[96:111]
	s_waitcnt lgkmcnt(0)
	v_mfma_f32_32x32x16_bf16 v[64:79], v[166:169], v[154:157], v[64:79]
	ds_read_b128 v[162:165], v212 offset:32768
	ds_read_b128 v[166:169], v212 offset:40960
	s_waitcnt lgkmcnt(0)
	v_mfma_f32_32x32x16_bf16 v[96:111], v[162:165], v[150:153], v[96:111]
	v_mfma_f32_32x32x16_bf16 v[64:79], v[166:169], v[150:153], v[64:79]
	ds_read_b128 v[162:165], v213 offset:32768
	ds_read_b128 v[166:169], v213 offset:40960
	s_waitcnt lgkmcnt(0)
	v_mfma_f32_32x32x16_bf16 v[96:111], v[162:165], v[146:149], v[96:111]
	v_mfma_f32_32x32x16_bf16 v[64:79], v[166:169], v[146:149], v[64:79]
	ds_read_b128 v[162:165], v215 offset:32768
	ds_read_b128 v[166:169], v215 offset:40960
	s_waitcnt lgkmcnt(0)
	v_mfma_f32_32x32x16_bf16 v[96:111], v[162:165], v[142:145], v[96:111]
	v_mfma_f32_32x32x16_bf16 v[64:79], v[166:169], v[142:145], v[64:79]
	ds_read_b128 v[162:165], v217 offset:32768
	ds_read_b128 v[166:169], v217 offset:40960
	s_waitcnt lgkmcnt(0)
	v_mfma_f32_32x32x16_bf16 v[96:111], v[162:165], v[138:141], v[96:111]
	v_mfma_f32_32x32x16_bf16 v[64:79], v[166:169], v[138:141], v[64:79]
	ds_read_b128 v[162:165], v214 offset:32768
	ds_read_b128 v[166:169], v214 offset:40960
	s_waitcnt lgkmcnt(0)
	v_mfma_f32_32x32x16_bf16 v[96:111], v[162:165], v[134:137], v[96:111]
	v_mfma_f32_32x32x16_bf16 v[64:79], v[166:169], v[134:137], v[64:79]
	ds_read_b128 v[162:165], v216 offset:32768
	ds_read_b128 v[166:169], v216 offset:40960
	s_waitcnt lgkmcnt(0)
	v_mfma_f32_32x32x16_bf16 v[96:111], v[162:165], v[130:133], v[96:111]
	v_mfma_f32_32x32x16_bf16 v[64:79], v[166:169], v[130:133], v[64:79]
	ds_read_b128 v[162:165], v219
	ds_read_b128 v[166:169], v219 offset:4096
	ds_read_b128 v[170:173], v204
	s_waitcnt lgkmcnt(0)
	v_mfma_f32_32x32x16_bf16 v[96:111], v[162:165], v[170:173], v[96:111]
	v_mfma_f32_32x32x16_bf16 v[64:79], v[166:169], v[170:173], v[64:79]
	ds_read_b128 v[162:165], v221
	ds_read_b128 v[166:169], v221 offset:4096
	ds_read_b128 v[170:173], v204 offset:1024
	s_waitcnt lgkmcnt(0)
	v_mfma_f32_32x32x16_bf16 v[96:111], v[162:165], v[170:173], v[96:111]
	v_mfma_f32_32x32x16_bf16 v[64:79], v[166:169], v[170:173], v[64:79]
	ds_read_b128 v[162:165], v223
	ds_read_b128 v[166:169], v223 offset:4096
	ds_read_b128 v[170:173], v204 offset:2048
	s_waitcnt lgkmcnt(0)
	v_mfma_f32_32x32x16_bf16 v[96:111], v[162:165], v[170:173], v[96:111]
	v_mfma_f32_32x32x16_bf16 v[64:79], v[166:169], v[170:173], v[64:79]
	ds_read_b128 v[162:165], v225
	ds_read_b128 v[166:169], v225 offset:4096
	ds_read_b128 v[170:173], v204 offset:3072
	s_waitcnt lgkmcnt(0)
	v_mfma_f32_32x32x16_bf16 v[96:111], v[162:165], v[170:173], v[96:111]
	v_exp_f32_e32 v162, v120
	v_exp_f32_e32 v163, v121
	v_exp_f32_e32 v164, v122
	v_exp_f32_e32 v165, v123
	v_add_f32_e32 v120, v80, v81
	v_add_f32_e32 v121, v88, v89
	v_add_f32_e32 v122, v112, v113
	v_mfma_f32_32x32x16_bf16 v[64:79], v[166:169], v[170:173], v[64:79]
	v_exp_f32_e32 v166, v124
	v_exp_f32_e32 v167, v125
	v_add_f32_e32 v123, v162, v163
	v_exp_f32_e32 v168, v126
	v_add_f32_e32 v120, v82, v120
	v_add_f32_e32 v121, v90, v121
	v_add_f32_e32 v122, v114, v122
	v_add_f32_e32 v123, v164, v123
	v_exp_f32_e32 v169, v127
	v_add_f32_e32 v120, v83, v120
	v_add_f32_e32 v121, v91, v121
	v_add_f32_e32 v122, v115, v122
	v_add_f32_e32 v123, v165, v123
	v_add_f32_e32 v120, v84, v120
	v_add_f32_e32 v121, v92, v121
	v_add_f32_e32 v122, v116, v122
	v_add_f32_e32 v123, v166, v123
	v_add_f32_e32 v120, v85, v120
	v_add_f32_e32 v121, v93, v121
	v_add_f32_e32 v122, v117, v122
	v_add_f32_e32 v123, v167, v123
	v_add_f32_e32 v120, v86, v120
	v_add_f32_e32 v121, v94, v121
	v_add_f32_e32 v122, v118, v122
	v_add_f32_e32 v123, v168, v123
	v_add_f32_e32 v120, v87, v120
	v_add_f32_e32 v121, v95, v121
	v_add_f32_e32 v122, v119, v122
	v_add_f32_e32 v123, v169, v123
	v_add_f32_e32 v120, v121, v120
	v_add_f32_e32 v121, v123, v122
	v_add_f32_e32 v239, v120, v121
	v_cvt_pk_bf16_f32 v124, v80, v81
	v_cvt_pk_bf16_f32 v125, v82, v83
	v_cvt_pk_bf16_f32 v126, v84, v85
	v_cvt_pk_bf16_f32 v127, v86, v87
	v_cvt_pk_bf16_f32 v120, v88, v89
	v_cvt_pk_bf16_f32 v121, v90, v91
	v_cvt_pk_bf16_f32 v122, v92, v93
	v_cvt_pk_bf16_f32 v123, v94, v95
	v_cvt_pk_bf16_f32 v112, v112, v113
	v_cvt_pk_bf16_f32 v113, v114, v115
	v_cvt_pk_bf16_f32 v114, v116, v117
	v_cvt_pk_bf16_f32 v115, v118, v119
	v_cvt_pk_bf16_f32 v116, v162, v163
	v_cvt_pk_bf16_f32 v117, v164, v165
	v_cvt_pk_bf16_f32 v118, v166, v167
	v_cvt_pk_bf16_f32 v119, v168, v169
	s_add_i32 s2, s20, 1
	s_min_i32 s2, s2, s23
	s_lshl_b32 s72, s2, 6
	s_mul_i32 s2, s72, s62
	s_mov_b32 s3, s73
	s_lshl_b64 s[2:3], s[2:3], 1
	s_add_u32 s24, s18, s2
	s_addc_u32 s25, s19, s3
	s_add_u32 s2, s16, s2
	s_addc_u32 s3, s17, s3
	global_load_dwordx4 v[162:165], v128, s[24:25]
	global_load_dwordx4 v[166:169], v182, s[24:25]
	global_load_dwordx4 v[170:173], v128, s[2:3]
	global_load_dwordx4 v[174:177], v182, s[2:3]
	s_lshl_b64 s[2:3], s[72:73], 7
	v_lshl_add_u64 v[80:81], v[184:185], 0, s[2:3]
	global_load_dwordx4 v[178:181], v[80:81], off
	ds_read_b64_tr_b16 v[80:81], v203 offset:0
	ds_read_b64_tr_b16 v[82:83], v203 offset:0x800
	ds_read_b64_tr_b16 v[84:85], v203 offset:0x1000
	ds_read_b64_tr_b16 v[86:87], v203 offset:0x1800
	ds_read_b64_tr_b16 v[88:89], v203 offset:0x2000
	ds_read_b64_tr_b16 v[90:91], v203 offset:0x2800
	ds_read_b64_tr_b16 v[92:93], v203 offset:0x3000
	ds_read_b64_tr_b16 v[94:95], v203 offset:0x3800
	s_waitcnt lgkmcnt(0)
	s_nop 0
	v_mfma_f32_32x32x16_bf16 v[0:15], v[80:83], v[124:127], v[0:15]
	v_max_f32_e32 v80, v64, v65
	v_max3_f32 v81, v96, v97, v98
	v_max3_f32 v80, v80, v66, v67
	v_max3_f32 v81, v81, v99, v100
	v_max3_f32 v80, v80, v68, v69
	v_mfma_f32_32x32x16_bf16 v[0:15], v[84:87], v[120:123], v[0:15]
	v_max3_f32 v81, v81, v101, v102
	v_max3_f32 v80, v80, v70, v71
	v_max3_f32 v81, v81, v103, v104
	v_max3_f32 v80, v80, v72, v73
	v_max3_f32 v81, v81, v105, v106
	v_max3_f32 v80, v80, v74, v75
	v_max3_f32 v81, v81, v107, v108
	v_mfma_f32_32x32x16_bf16 v[0:15], v[88:91], v[112:115], v[0:15]
	v_max3_f32 v80, v80, v76, v77
	v_max3_f32 v81, v81, v109, v110
	v_max3_f32 v80, v80, v78, v79
	v_max3_f32 v194, v81, v111, v80
	ds_read_b64_tr_b16 v[80:81], v203 offset:0x200
	ds_read_b64_tr_b16 v[82:83], v203 offset:0xa00
	ds_read_b64_tr_b16 v[84:85], v203 offset:0x1200
	v_mfma_f32_32x32x16_bf16 v[0:15], v[92:95], v[116:119], v[0:15]
	ds_read_b64_tr_b16 v[86:87], v203 offset:0x1a00
	ds_read_b64_tr_b16 v[88:89], v203 offset:0x2200
	ds_read_b64_tr_b16 v[90:91], v203 offset:0x2a00
	ds_read_b64_tr_b16 v[92:93], v203 offset:0x3200
	ds_read_b64_tr_b16 v[94:95], v203 offset:0x3a00
	s_waitcnt lgkmcnt(0)
	v_mfma_f32_32x32x16_bf16 v[48:63], v[80:83], v[124:127], v[48:63]
	v_mov_b32_e32 v80, v194
	s_nop 1
	v_permlane32_swap_b32_e32 v194, v80
	v_max_f32_e32 v80, v194, v80
	v_sub_f32_e32 v81, v80, v227
	v_mfma_f32_32x32x16_bf16 v[48:63], v[84:87], v[120:123], v[48:63]
	v_cmp_ge_f32_e32 vcc, s34, v81
	v_mov_b32_e32 v200, 1.0
	s_cmp_eq_u64 vcc, exec
	s_cbranch_scc0 .Lmla_resc_1

.LBB0_880:
	v_add_u32_e32 v21, 32, v185
	v_and_b32_e32 v17, 0xfffff0, v185
	v_lshlrev_b32_e32 v18, 1, v185
	v_and_b32_e32 v22, 0xfffff0, v21
	v_lshlrev_b32_e32 v23, 1, v21
	v_and_b32_e32 v16, 63, v184
	v_and_or_b32 v17, v18, 8, v17
	v_and_or_b32 v22, v23, 8, v22
	v_lshrrev_b32_e32 v17, 1, v17
	v_lshrrev_b32_e32 v19, 5, v186
	v_lshrrev_b32_e32 v22, 1, v22
	v_lshlrev_b32_e32 v23, 4, v16
	v_lshrrev_b32_e32 v18, 1, v185
	v_or_b32_e32 v17, v17, v19
	v_and_b32_e32 v20, 3, v185
	v_or_b32_e32 v19, v22, v19
	v_lshlrev_b32_e32 v22, 3, v16
	v_and_b32_e32 v23, 0xc0, v23
	v_lshlrev_b32_e32 v16, 1, v16
	v_and_or_b32 v18, v18, 4, v20
	v_lshlrev_b32_e32 v20, 1, v186
	v_and_or_b32 v23, v22, 24, v23
	v_and_b32_e32 v16, 32, v16
	v_and_b32_e32 v22, 0x100, v22
	v_lshlrev_b32_e32 v17, 9, v17
	v_lshlrev_b32_e32 v18, 6, v18
	v_or3_b32 v114, v23, v16, v22
	v_and_b32_e32 v16, 48, v20
	v_or3_b32 v17, v17, v18, v16
	v_add_u32_e32 v212, 0, v17
	v_lshrrev_b32_e32 v17, 3, v212
	v_xor_b32_e32 v17, v17, v212
	v_and_b32_e32 v17, 0x100, v17
	v_xor_b32_e32 v212, v212, v17
	v_lshlrev_b32_e32 v17, 3, v17
	v_xor_b32_e32 v212, v212, v17
	v_lshlrev_b32_e32 v19, 9, v19
	v_cvt_pk_bf16_f32 v138, v176, v177
	v_cvt_pk_bf16_f32 v139, v170, v171
	v_cvt_pk_bf16_f32 v140, v164, v165
	v_cvt_pk_bf16_f32 v141, v144, v145
	v_cvt_pk_bf16_f32 v154, v142, v143
	v_cvt_pk_bf16_f32 v155, v136, v137
	v_cvt_pk_bf16_f32 v156, v134, v135
	v_cvt_pk_bf16_f32 v157, v132, v133
	v_cvt_pk_bf16_f32 v158, v130, v131
	v_cvt_pk_bf16_f32 v159, v126, v127
	v_cvt_pk_bf16_f32 v160, v124, v125
	v_cvt_pk_bf16_f32 v161, v122, v123
	v_cvt_pk_bf16_f32 v150, v120, v121
	v_cvt_pk_bf16_f32 v151, v118, v119
	v_cvt_pk_bf16_f32 v152, v116, v117
	v_cvt_pk_bf16_f32 v153, v112, v113
	v_cvt_pk_bf16_f32 v146, v108, v109
	v_cvt_pk_bf16_f32 v147, v110, v111
	v_cvt_pk_bf16_f32 v148, v104, v105
	v_cvt_pk_bf16_f32 v149, v106, v107
	v_cvt_pk_bf16_f32 v142, v100, v101
	v_cvt_pk_bf16_f32 v143, v102, v103
	v_cvt_pk_bf16_f32 v144, v96, v97
	v_cvt_pk_bf16_f32 v145, v98, v99
	v_cvt_pk_bf16_f32 v134, v92, v93
	v_cvt_pk_bf16_f32 v135, v94, v95
	v_cvt_pk_bf16_f32 v136, v88, v89
	v_cvt_pk_bf16_f32 v137, v90, v91
	v_cvt_pk_bf16_f32 v130, v84, v85
	v_cvt_pk_bf16_f32 v131, v86, v87
	v_cvt_pk_bf16_f32 v132, v80, v81
	v_cvt_pk_bf16_f32 v133, v82, v83
	s_waitcnt vmcnt(0)
	ds_write_b128 v212, v[8:11]
	v_lshlrev_b32_e32 v8, 8, v185
	v_and_b32_e32 v9, 0x70, v184
	v_or3_b32 v16, v19, v18, v16
	v_bitop3_b32 v8, v20, v8, v9 bitop3:0xde
	v_add_u32_e32 v213, 0, v16
	v_lshrrev_b32_e32 v16, 3, v213
	v_xor_b32_e32 v16, v16, v213
	v_and_b32_e32 v16, 0x100, v16
	v_xor_b32_e32 v213, v213, v16
	v_lshlrev_b32_e32 v16, 3, v16
	v_xor_b32_e32 v213, v213, v16
	v_add_u32_e32 v214, 0, v8
	ds_write_b128 v213, v[12:15]
	ds_write_b128 v214, v[4:7] offset:32768
	v_lshlrev_b32_e32 v4, 8, v21
	v_bitop3_b32 v4, v20, v4, v9 bitop3:0xde
	v_add_u32_e32 v215, 0, v4
	ds_write_b128 v215, v[0:3] offset:32768
	v_lshlrev_b32_e32 v0, 4, v163
	v_lshlrev_b32_e32 v56, 8, v163
	v_and_b32_e32 v57, 0x70, v0
	v_bitop3_b32 v0, v162, v56, v57 bitop3:0xde
	v_add_u32_e32 v216, 0, v0
	s_waitcnt lgkmcnt(0)
	s_barrier
	s_add_u32 s16, s10, s96
	s_addc_u32 s17, s11, s97
	s_add_u32 s18, s8, s96
	s_addc_u32 s19, s9, s97
	global_load_dwordx4 v[178:181], v128, s[16:17]
	global_load_dwordx4 v[182:185], v198, s[16:17]
	global_load_dwordx4 v[186:189], v128, s[18:19]
	global_load_dwordx4 v[190:193], v198, s[18:19]
	ds_read_b128 v[16:19], v216 offset:32768
	ds_read_b128 v[20:23], v216 offset:40960
	s_waitcnt lgkmcnt(1)
	v_mfma_f32_32x32x16_bf16 v[32:47], v[16:19], v[138:141], 0
	v_or_b32_e32 v48, 32, v162
	v_bitop3_b32 v48, v48, v56, v57 bitop3:0xde
	v_add_u32_e32 v218, 0, v48
	ds_read_b128 v[48:51], v218 offset:32768
	ds_read_b128 v[52:55], v218 offset:40960
	s_cmp_lg_u32 0, -1
	s_cselect_b32 s53, 0, 0
	s_add_u32 s16, s10, s96
	s_waitcnt lgkmcnt(2)
	v_mfma_f32_32x32x16_bf16 v[16:31], v[20:23], v[138:141], 0
	s_addc_u32 s17, s11, s97
	v_mov_b32_e32 v199, v129
	s_add_u32 s18, s8, s96
	s_addc_u32 s19, s9, s97
	s_add_u32 s2, s16, s96
	s_addc_u32 s3, s17, s97
	s_waitcnt lgkmcnt(1)
	v_mfma_f32_32x32x16_bf16 v[32:47], v[48:51], v[154:157], v[32:47]
	v_or_b32_e32 v48, 64, v162
	v_bitop3_b32 v48, v48, v56, v57 bitop3:0xde
	v_add_u32_e32 v219, 0, v48
	v_lshl_add_u64 v[64:65], s[2:3], 0, v[128:129]
	s_mov_b32 s72, s73
	s_mov_b32 s74, s73
	s_mov_b32 s75, s73
	s_waitcnt lgkmcnt(0)
	v_mfma_f32_32x32x16_bf16 v[16:31], v[52:55], v[154:157], v[16:31]
	ds_read_b128 v[48:51], v219 offset:32768
	ds_read_b128 v[52:55], v219 offset:40960
	s_mov_b32 s76, s73
	s_mov_b32 s77, s73
	s_mov_b32 s78, s73
	s_mov_b32 s79, s73
	s_mov_b32 s80, s73
	s_mov_b32 s81, s73
	s_waitcnt lgkmcnt(1)
	v_mfma_f32_32x32x16_bf16 v[32:47], v[48:51], v[158:161], v[32:47]
	v_or_b32_e32 v48, 0x60, v162
	v_bitop3_b32 v48, v48, v56, v57 bitop3:0xde
	v_add_u32_e32 v220, 0, v48
	s_mov_b32 s82, s73
	s_mov_b32 s83, s73
	s_mov_b32 s84, s73
	s_mov_b32 s85, s73
	s_waitcnt lgkmcnt(0)
	v_mfma_f32_32x32x16_bf16 v[16:31], v[52:55], v[158:161], v[16:31]
	ds_read_b128 v[48:51], v220 offset:32768
	ds_read_b128 v[52:55], v220 offset:40960
	s_mov_b32 s86, s73
	s_mov_b32 s87, s73
	v_mov_b64_e32 v[0:1], s[72:73]
	v_mov_b64_e32 v[14:15], s[86:87]
	v_add_u32_e32 v209, s53, v114
	v_mov_b64_e32 v[2:3], s[74:75]
	s_waitcnt lgkmcnt(1)
	v_mfma_f32_32x32x16_bf16 v[32:47], v[48:51], v[150:153], v[32:47]
	v_or_b32_e32 v48, 0x80, v162
	v_bitop3_b32 v48, v48, v56, v57 bitop3:0xde
	v_add_u32_e32 v221, 0, v48
	v_mov_b64_e32 v[4:5], s[76:77]
	v_mov_b64_e32 v[6:7], s[78:79]
	v_mov_b64_e32 v[8:9], s[80:81]
	v_mov_b64_e32 v[10:11], s[82:83]
	s_waitcnt lgkmcnt(0)
	v_mfma_f32_32x32x16_bf16 v[16:31], v[52:55], v[150:153], v[16:31]
	ds_read_b128 v[48:51], v221 offset:32768
	ds_read_b128 v[52:55], v221 offset:40960
	v_mov_b64_e32 v[12:13], s[84:85]
	s_mov_b32 s39, 4
	v_mov_b32_e32 v217, 0
	v_readlane_b32 s80, v255, 48
	s_movk_i32 s79, 0xff
	s_movk_i32 s84, 0xffe0
	s_waitcnt lgkmcnt(1)
	v_mfma_f32_32x32x16_bf16 v[32:47], v[48:51], v[146:149], v[32:47]
	v_or_b32_e32 v48, 0xa0, v162
	v_bitop3_b32 v48, v48, v56, v57 bitop3:0xde
	v_add_u32_e32 v222, 0, v48
	s_waitcnt lgkmcnt(0)
	v_mfma_f32_32x32x16_bf16 v[16:31], v[52:55], v[146:149], v[16:31]
	ds_read_b128 v[48:51], v222 offset:32768
	ds_read_b128 v[52:55], v222 offset:40960
	s_waitcnt lgkmcnt(1)
	v_mfma_f32_32x32x16_bf16 v[32:47], v[48:51], v[142:145], v[32:47]
	v_or_b32_e32 v48, 0xc0, v162
	v_bitop3_b32 v48, v48, v56, v57 bitop3:0xde
	v_add_u32_e32 v224, 0, v48
	s_waitcnt lgkmcnt(0)
	v_mfma_f32_32x32x16_bf16 v[16:31], v[52:55], v[142:145], v[16:31]
	ds_read_b128 v[48:51], v224 offset:32768
	ds_read_b128 v[52:55], v224 offset:40960
	s_waitcnt lgkmcnt(1)
	v_mfma_f32_32x32x16_bf16 v[32:47], v[48:51], v[134:137], v[32:47]
	v_or_b32_e32 v48, 0xe0, v162
	v_bitop3_b32 v48, v48, v56, v57 bitop3:0xde
	v_add_u32_e32 v223, 0, v48
	s_waitcnt lgkmcnt(0)
	v_mfma_f32_32x32x16_bf16 v[16:31], v[52:55], v[134:137], v[16:31]
	ds_read_b128 v[48:51], v223 offset:32768
	ds_read_b128 v[52:55], v223 offset:40960
	global_load_dwordx4 v[162:165], v[64:65], off
	v_lshl_add_u64 v[64:65], s[2:3], 0, v[198:199]
	s_waitcnt lgkmcnt(1)
	v_mfma_f32_32x32x16_bf16 v[32:47], v[48:51], v[130:133], v[32:47]
	global_load_dwordx4 v[166:169], v[64:65], off
	s_waitcnt lgkmcnt(0)
	v_mfma_f32_32x32x16_bf16 v[16:31], v[52:55], v[130:133], v[16:31]
	s_nop 8
	s_add_u32 s16, s18, s96
	s_addc_u32 s17, s19, s97
	v_lshl_add_u64 v[64:65], s[16:17], 0, v[128:129]
	global_load_dwordx4 v[170:173], v[64:65], off
	v_lshl_add_u64 v[64:65], s[16:17], 0, v[198:199]
	global_load_dwordx4 v[174:177], v[64:65], off
	s_and_b64 s[2:3], s[14:15], exec
	s_cselect_b32 s14, 3, 35
	v_exp_f32_e32 v64, v32
	v_exp_f32_e32 v65, v33
	v_exp_f32_e32 v66, v34
	v_exp_f32_e32 v67, v35
	v_exp_f32_e32 v68, v36
	v_exp_f32_e32 v69, v37
	v_exp_f32_e32 v70, v38
	v_exp_f32_e32 v71, v39
	v_exp_f32_e32 v72, v40
	v_exp_f32_e32 v73, v41
	v_exp_f32_e32 v74, v42
	v_exp_f32_e32 v80, v16
	v_exp_f32_e32 v81, v17
	v_exp_f32_e32 v75, v43
	v_exp_f32_e32 v76, v44
	v_exp_f32_e32 v77, v45
	v_exp_f32_e32 v78, v46
	v_exp_f32_e32 v79, v47
	v_exp_f32_e32 v82, v18
	v_exp_f32_e32 v83, v19
	v_lshl_add_u64 v[16:17], s[12:13], 0, v[128:129]
	v_lshl_add_u64 v[18:19], s[12:13], 0, v[198:199]
	v_exp_f32_e32 v94, v30
	v_exp_f32_e32 v95, v31
	v_exp_f32_e32 v92, v28
	v_exp_f32_e32 v93, v29
	v_exp_f32_e32 v196, v26
	v_exp_f32_e32 v197, v27
	v_exp_f32_e32 v194, v24
	v_exp_f32_e32 v195, v25
	v_exp_f32_e32 v86, v22
	v_exp_f32_e32 v87, v23
	v_exp_f32_e32 v84, v20
	v_exp_f32_e32 v85, v21
	s_addk_i32 s53, 0x4000
	v_lshl_add_u64 v[200:201], s[64:65], 0, v[16:17]
	v_lshl_add_u64 v[202:203], s[64:65], 0, v[18:19]
	v_lshl_add_u64 v[204:205], s[66:67], 0, v[16:17]
	v_lshl_add_u64 v[206:207], s[66:67], 0, v[18:19]
	v_mov_b64_e32 v[62:63], v[14:15]
	v_mov_b64_e32 v[46:47], v[14:15]
	v_mov_b64_e32 v[30:31], v[14:15]
	v_add_u32_e32 v211, s53, v114
	v_mov_b64_e32 v[60:61], v[12:13]
	v_mov_b64_e32 v[58:59], v[10:11]
	v_mov_b64_e32 v[56:57], v[8:9]
	v_mov_b64_e32 v[54:55], v[6:7]
	v_mov_b64_e32 v[52:53], v[4:5]
	v_mov_b64_e32 v[50:51], v[2:3]
	v_mov_b64_e32 v[48:49], v[0:1]
	v_mov_b64_e32 v[44:45], v[12:13]
	v_mov_b64_e32 v[42:43], v[10:11]
	v_mov_b64_e32 v[40:41], v[8:9]
	v_mov_b64_e32 v[38:39], v[6:7]
	v_mov_b64_e32 v[36:37], v[4:5]
	v_mov_b64_e32 v[34:35], v[2:3]
	v_mov_b64_e32 v[32:33], v[0:1]
	v_mov_b64_e32 v[28:29], v[12:13]
	v_mov_b64_e32 v[26:27], v[10:11]
	v_mov_b64_e32 v[24:25], v[8:9]
	v_mov_b64_e32 v[22:23], v[6:7]
	v_mov_b64_e32 v[20:21], v[4:5]
	v_mov_b64_e32 v[18:19], v[2:3]
	v_mov_b64_e32 v[16:17], v[0:1]
	s_waitcnt vmcnt(4)
	ds_write_b128 v212, v[178:181] offset:16384
	ds_write_b128 v213, v[182:185] offset:16384
	ds_write_b128 v214, v[186:189] offset:49152
	ds_write_b128 v215, v[190:193] offset:49152
	s_mov_b32 s53, 0x38e38e39
	s_waitcnt lgkmcnt(0)
	s_barrier
	.p2alignl 3, 3212836864
